# speedup vs baseline: 1.0118x; 1.0118x over previous
_Z15qkv_gemm_kernelPKDF16_S0_PKfS2_S2_PDF16_S3_S3_:
	s_load_dwordx8 s[8:15], s[0:1], 0x0
	s_load_dwordx2 s[44:45], s[0:1], 0x20
	s_ashr_i32 s3, s2, 3
	s_lshl_b32 s2, s2, 5
	v_lshlrev_b32_e32 v1, 4, v0
	v_and_b32_e32 v2, 32, v0
	s_and_b32 s2, s2, 0xe0
	v_bfe_u32 v3, v0, 2, 4
	v_bitop3_b32 v2, v1, v2, 48 bitop3:0x6c
	v_lshrrev_b32_e32 v104, 3, v0
	s_add_i32 s2, s2, s3
	v_and_or_b32 v2, v0, 64, v2
	v_and_or_b32 v4, v104, 48, v3
	s_ashr_i32 s33, s2, 4
	s_and_b32 s36, s3, 15
	v_lshl_or_b32 v100, v4, 11, v2
	v_or_b32_e32 v4, 64, v104
	s_movk_i32 s2, 0x70
	v_and_or_b32 v3, v4, s2, v3
	s_lshl_b32 s2, s36, 19
	v_or_b32_e32 v106, 0xc000, v1
	v_lshl_or_b32 v103, v3, 11, v2
	s_waitcnt lgkmcnt(0)
	v_readfirstlane_b32 s46, v0
	v_bfe_u32 v187, v0, 4, 2
	v_lshlrev_b32_e32 v187, 4, v187
	s_lshr_b32 s46, s46, 8
	s_mul_i32 s46, s46, 48
	s_mul_i32 s47, s33, 0xc0
	s_add_i32 s46, s46, s47
	s_add_i32 s47, s46, 0
	s_lshr_b32 s48, s47, 10
	s_and_b32 s47, s47, 0x3ff
	s_lshl_b32 s47, s47, 2
	s_cmp_eq_u32 s48, 1
	s_cselect_b32 s50, s14, s44
	s_cselect_b32 s51, s15, s45
	s_cmp_eq_u32 s48, 0
	s_cselect_b32 s50, s12, s50
	s_cselect_b32 s51, s13, s51
	s_add_u32 s50, s50, s47
	s_addc_u32 s51, s51, 0
	global_load_dwordx4 v[188:191], v187, s[50:51]
	s_add_i32 s47, s46, 16
	s_lshr_b32 s48, s47, 10
	s_and_b32 s47, s47, 0x3ff
	s_lshl_b32 s47, s47, 2
	s_cmp_eq_u32 s48, 1
	s_cselect_b32 s50, s14, s44
	s_cselect_b32 s51, s15, s45
	s_cmp_eq_u32 s48, 0
	s_cselect_b32 s50, s12, s50
	s_cselect_b32 s51, s13, s51
	s_add_u32 s50, s50, s47
	s_addc_u32 s51, s51, 0
	global_load_dwordx4 v[192:195], v187, s[50:51]
	s_add_i32 s47, s46, 32
	s_lshr_b32 s48, s47, 10
	s_and_b32 s47, s47, 0x3ff
	s_lshl_b32 s47, s47, 2
	s_cmp_eq_u32 s48, 1
	s_cselect_b32 s50, s14, s44
	s_cselect_b32 s51, s15, s45
	s_cmp_eq_u32 s48, 0
	s_cselect_b32 s50, s12, s50
	s_cselect_b32 s51, s13, s51
	s_add_u32 s50, s50, s47
	s_addc_u32 s51, s51, 0
	global_load_dwordx4 v[196:199], v187, s[50:51]
	s_add_i32 s47, s46, 96
	s_lshr_b32 s48, s47, 10
	s_and_b32 s47, s47, 0x3ff
	s_lshl_b32 s47, s47, 2
	s_cmp_eq_u32 s48, 1
	s_cselect_b32 s50, s14, s44
	s_cselect_b32 s51, s15, s45
	s_cmp_eq_u32 s48, 0
	s_cselect_b32 s50, s12, s50
	s_cselect_b32 s51, s13, s51
	s_add_u32 s50, s50, s47
	s_addc_u32 s51, s51, 0
	global_load_dwordx4 v[200:203], v187, s[50:51]
	s_add_i32 s47, s46, 112
	s_lshr_b32 s48, s47, 10
	s_and_b32 s47, s47, 0x3ff
	s_lshl_b32 s47, s47, 2
	s_cmp_eq_u32 s48, 1
	s_cselect_b32 s50, s14, s44
	s_cselect_b32 s51, s15, s45
	s_cmp_eq_u32 s48, 0
	s_cselect_b32 s50, s12, s50
	s_cselect_b32 s51, s13, s51
	s_add_u32 s50, s50, s47
	s_addc_u32 s51, s51, 0
	global_load_dwordx4 v[204:207], v187, s[50:51]
	s_add_i32 s47, s46, 128
	s_lshr_b32 s48, s47, 10
	s_and_b32 s47, s47, 0x3ff
	s_lshl_b32 s47, s47, 2
	s_cmp_eq_u32 s48, 1
	s_cselect_b32 s50, s14, s44
	s_cselect_b32 s51, s15, s45
	s_cmp_eq_u32 s48, 0
	s_cselect_b32 s50, s12, s50
	s_cselect_b32 s51, s13, s51
	s_add_u32 s50, s50, s47
	s_addc_u32 s51, s51, 0
	global_load_dwordx4 v[208:211], v187, s[50:51]
	s_add_u32 s2, s8, s2
	v_mov_b32_e32 v2, v100
	v_readfirstlane_b32 s6, v106
	s_addc_u32 s3, s9, 0
	s_mov_b32 m0, s6
	v_or_b32_e32 v107, 0xe000, v1
	s_mul_i32 s5, s33, 0x60000
	global_load_lds_dwordx4 v2, s[2:3]
	v_mov_b32_e32 v2, v103
	v_readfirstlane_b32 s6, v107
	s_mul_hi_i32 s4, s33, 0x60000
	v_readfirstlane_b32 s19, v0
	s_mov_b32 m0, s6
	s_add_u32 s16, s10, s5
	global_load_lds_dwordx4 v2, s[2:3]
	s_addc_u32 s17, s11, s4
	s_lshr_b32 s18, s19, 8
	v_mov_b32_e32 v2, v100
	v_readfirstlane_b32 s4, v1
	s_cmpk_lt_u32 s19, 0x100
	s_mov_b32 m0, s4
	s_cselect_b64 vcc, -1, 0
	global_load_lds_dwordx4 v2, s[16:17]
	v_add_u32_e32 v2, 0x1b000, v1
	v_or_b32_e32 v4, 0x2000, v1
	v_cndmask_b32_e32 v101, v100, v103, vcc
	v_cndmask_b32_e32 v111, v2, v4, vcc
	v_mov_b32_e32 v3, v101
	v_readfirstlane_b32 s4, v111
	s_mov_b32 m0, s4
	v_or_b32_e32 v112, 0x10000, v1
	global_load_lds_dwordx4 v3, s[16:17]
	s_add_u32 s4, s2, 0x40000
	v_mov_b32_e32 v3, v100
	v_readfirstlane_b32 s6, v112
	s_addc_u32 s5, s3, 0
	s_mov_b32 m0, s6
	v_or_b32_e32 v113, 0x12000, v1
	global_load_lds_dwordx4 v3, s[4:5]
	v_mov_b32_e32 v3, v103
	v_readfirstlane_b32 s6, v113
	s_mov_b32 m0, s6
	v_add_u32_e32 v115, 0x3000, v1
	v_add_u32_e32 v4, 0x5000, v1
	global_load_lds_dwordx4 v3, s[4:5]
	s_add_u32 s4, s16, 0x30000
	v_mov_b32_e32 v3, v100
	v_readfirstlane_b32 s6, v115
	v_cndmask_b32_e32 v116, v2, v4, vcc
	s_addc_u32 s5, s17, 0
	s_mov_b32 m0, s6
	v_readfirstlane_b32 s6, v116
	global_load_lds_dwordx4 v3, s[4:5]
	v_mov_b32_e32 v3, v101
	s_mov_b32 m0, s6
	s_cmp_lg_u32 s18, 1
	global_load_lds_dwordx4 v3, s[4:5]
	s_load_dwordx8 s[4:11], s[0:1], 0x20
	s_mov_b32 s0, 0x10000
	s_cbranch_scc1 .LBB1_2
	s_barrier

.LBB1_6:
	s_mul_i32 s18, s33, 0xc0
	s_add_i32 s0, s37, s18
	s_lshl_b32 s19, s40, 5
	s_lshr_b32 s20, s37, 6
	s_ashr_i32 s2, s0, 10
	s_and_b32 s1, s0, 0x3f0
	s_cmpk_lt_u32 s0, 0x400
	v_and_b32_e32 v107, 12, v102
	s_cselect_b64 vcc, -1, 0
	s_cmp_eq_u32 s2, 1
	v_or_b32_e32 v94, s1, v107
	s_cselect_b32 s3, s14, s4
	s_cselect_b32 s16, s15, s5
	s_and_b64 s[0:1], vcc, exec
	v_mov_b32_e32 v95, 0x3e38aa3b
	s_cselect_b32 s1, s13, s16
	s_cselect_b32 s0, s12, s3
	v_lshlrev_b32_e32 v94, 2, v94
	s_barrier
	v_cndmask_b32_e32 v102, 1.0, v95, vcc
	v_mov_b32_e32 v94, v188
	v_mov_b32_e32 v95, v189
	v_mov_b32_e32 v96, v190
	v_mov_b32_e32 v97, v191
	v_lshrrev_b32_e32 v103, 1, v0
	v_bfe_u32 v106, v0, 3, 1
	v_and_b32_e32 v108, 3, v0
	v_and_or_b32 v103, v103, 2, v106
	v_lshl_or_b32 v110, v103, 2, v108
	v_or_b32_e32 v103, s19, v110
	v_lshlrev_b32_e32 v109, 1, v103
	s_cmp_gt_i32 s2, 1
	v_and_or_b32 v106, s37, 48, v107
	s_cselect_b64 s[2:3], -1, 0
	s_mov_b64 s[0:1], -1
	s_mul_i32 s20, s20, 0x9000
	v_lshlrev_b32_e32 v108, 1, v106
	s_and_b64 vcc, exec, s[2:3]
	s_waitcnt vmcnt(0)
	v_add_f32_e32 v103, v94, v98
	v_add_f32_e32 v98, v96, v100
	v_add_f32_e32 v99, v95, v99
	v_pk_mov_b32 v[98:99], v[98:99], v[98:99] op_sel:[1,0]
	v_add_f32_e32 v101, v97, v101
	v_pk_mul_f32 v[98:99], v[102:103], v[98:99] op_sel_hi:[0,1]
	v_fma_mixlo_f16 v100, v102, v103, 0
	v_fma_mixlo_f16 v101, v102, v101, 0
	v_cvt_pk_f16_f32 v111, v98, v99
	s_cbranch_vccz .LBB1_8
	v_mul_u32_u24_e32 v98, 0x210, v106
	v_add3_u32 v98, s20, v109, v98
	ds_write_b16 v98, v100
	ds_write_b16 v98, v111 offset:528
	ds_write_b16_d16_hi v98, v111 offset:1056
	ds_write_b16 v98, v101 offset:1584
	s_mov_b64 s[0:1], 0

.LBB1_22:
	s_add_i32 s0, s39, s18
	s_lshr_b32 s16, s39, 6
	s_ashr_i32 s17, s0, 10
	s_and_b32 s1, s0, 0x3f0
	s_cmpk_lt_u32 s0, 0x400
	s_cselect_b64 vcc, -1, 0
	s_cmp_eq_u32 s17, 1
	v_or_b32_e32 v82, s1, v107
	s_cselect_b32 s2, s14, s4
	s_cselect_b32 s3, s15, s5
	s_and_b64 s[0:1], vcc, exec
	v_mov_b32_e32 v83, 0x3e38aa3b
	s_cselect_b32 s1, s13, s3
	s_cselect_b32 s0, s12, s2
	v_lshlrev_b32_e32 v82, 2, v82
	v_cndmask_b32_e32 v86, 1.0, v83, vcc
	v_mov_b32_e32 v82, v192
	v_mov_b32_e32 v83, v193
	v_mov_b32_e32 v84, v194
	v_mov_b32_e32 v85, v195
	s_cmp_gt_i32 s17, 1
	v_and_or_b32 v94, s39, 48, v107
	s_mul_i32 s16, s16, 0x9000
	s_cselect_b64 s[2:3], -1, 0
	s_cmp_lt_i32 s17, 2
	s_mov_b64 s[0:1], -1
	s_waitcnt vmcnt(0)
	v_add_f32_e32 v95, v82, v78
	v_add_f32_e32 v78, v84, v80
	v_add_f32_e32 v87, v83, v79
	v_fma_mixlo_f16 v79, v86, v95, 0
	v_pk_mov_b32 v[96:97], v[86:87], v[78:79] op_sel:[1,0]
	v_add_f32_e32 v80, v85, v81
	v_pk_mul_f32 v[96:97], v[86:87], v[96:97] op_sel_hi:[0,1]
	v_fma_mixlo_f16 v80, v86, v80, 0
	v_cvt_pk_f16_f32 v81, v96, v97
	s_cbranch_scc1 .LBB1_24
	v_mul_u32_u24_e32 v78, 0x210, v94
	v_add3_u32 v78, s16, v109, v78
	s_mov_b64 s[0:1], 0
	ds_write_b16 v78, v79
	ds_write_b16 v78, v81 offset:528
	ds_write_b16_d16_hi v78, v81 offset:1056
	ds_write_b16 v78, v80 offset:1584

.LBB1_38:
	s_add_i32 s0, s38, s18
	s_lshr_b32 s16, s38, 6
	s_ashr_i32 s17, s0, 10
	s_and_b32 s1, s0, 0x3f0
	s_cmpk_lt_u32 s0, 0x400
	s_cselect_b64 vcc, -1, 0
	s_cmp_eq_u32 s17, 1
	v_or_b32_e32 v66, s1, v107
	s_cselect_b32 s2, s14, s4
	s_cselect_b32 s3, s15, s5
	s_and_b64 s[0:1], vcc, exec
	v_mov_b32_e32 v67, 0x3e38aa3b
	s_cselect_b32 s1, s13, s3
	s_cselect_b32 s0, s12, s2
	v_lshlrev_b32_e32 v66, 2, v66
	v_cndmask_b32_e32 v70, 1.0, v67, vcc
	v_mov_b32_e32 v66, v196
	v_mov_b32_e32 v67, v197
	v_mov_b32_e32 v68, v198
	v_mov_b32_e32 v69, v199
	s_cmp_gt_i32 s17, 1
	v_and_or_b32 v72, s38, 48, v107
	s_mul_i32 s16, s16, 0x9000
	s_cselect_b64 s[2:3], -1, 0
	s_cmp_lt_i32 s17, 2
	s_mov_b64 s[0:1], -1
	s_waitcnt vmcnt(0)
	v_add_f32_e32 v73, v66, v62
	v_add_f32_e32 v62, v68, v64
	v_add_f32_e32 v71, v67, v63
	v_fma_mixlo_f16 v63, v70, v73, 0
	v_pk_mov_b32 v[74:75], v[70:71], v[62:63] op_sel:[1,0]
	v_add_f32_e32 v64, v69, v65
	v_pk_mul_f32 v[74:75], v[70:71], v[74:75] op_sel_hi:[0,1]
	v_fma_mixlo_f16 v64, v70, v64, 0
	v_cvt_pk_f16_f32 v65, v74, v75
	s_cbranch_scc1 .LBB1_40
	v_mul_u32_u24_e32 v62, 0x210, v72
	v_add3_u32 v62, s16, v109, v62
	s_mov_b64 s[0:1], 0
	ds_write_b16 v62, v63
	ds_write_b16 v62, v65 offset:528
	ds_write_b16_d16_hi v62, v65 offset:1056
	ds_write_b16 v62, v64 offset:1584

.LBB1_54:
	s_add_i32 s2, s37, 0x60
	s_add_i32 s0, s2, s18
	s_lshr_b32 s16, s2, 6
	s_ashr_i32 s17, s0, 10
	s_and_b32 s1, s0, 0x3f0
	s_cmpk_lt_u32 s0, 0x400
	s_cselect_b64 vcc, -1, 0
	s_cmp_eq_u32 s17, 1
	v_or_b32_e32 v50, s1, v107
	s_cselect_b32 s3, s14, s4
	s_cselect_b32 s19, s15, s5
	s_and_b64 s[0:1], vcc, exec
	v_mov_b32_e32 v51, 0x3e38aa3b
	s_cselect_b32 s1, s13, s19
	s_cselect_b32 s0, s12, s3
	v_lshlrev_b32_e32 v50, 2, v50
	v_cndmask_b32_e32 v54, 1.0, v51, vcc
	v_mov_b32_e32 v50, v200
	v_mov_b32_e32 v51, v201
	v_mov_b32_e32 v52, v202
	v_mov_b32_e32 v53, v203
	s_cmp_gt_i32 s17, 1
	v_and_or_b32 v56, s2, 48, v107
	s_mul_i32 s16, s16, 0x9000
	s_cselect_b64 s[2:3], -1, 0
	s_cmp_lt_i32 s17, 2
	s_mov_b64 s[0:1], -1
	s_waitcnt vmcnt(0)
	v_add_f32_e32 v57, v50, v46
	v_add_f32_e32 v46, v52, v48
	v_add_f32_e32 v55, v51, v47
	v_fma_mixlo_f16 v47, v54, v57, 0
	v_pk_mov_b32 v[58:59], v[54:55], v[46:47] op_sel:[1,0]
	v_add_f32_e32 v48, v53, v49
	v_pk_mul_f32 v[58:59], v[54:55], v[58:59] op_sel_hi:[0,1]
	v_fma_mixlo_f16 v48, v54, v48, 0
	v_cvt_pk_f16_f32 v49, v58, v59
	s_cbranch_scc1 .LBB1_56
	v_mul_u32_u24_e32 v46, 0x210, v56
	v_add3_u32 v46, s16, v109, v46
	s_mov_b64 s[0:1], 0
	ds_write_b16 v46, v47
	ds_write_b16 v46, v49 offset:528
	ds_write_b16_d16_hi v46, v49 offset:1056
	ds_write_b16 v46, v48 offset:1584

.LBB1_70:
	s_add_i32 s2, s37, 0x70
	s_add_i32 s0, s2, s18
	s_lshr_b32 s16, s2, 6
	s_ashr_i32 s17, s0, 10
	s_and_b32 s1, s0, 0x3f0
	s_cmpk_lt_u32 s0, 0x400
	s_cselect_b64 vcc, -1, 0
	s_cmp_eq_u32 s17, 1
	v_or_b32_e32 v34, s1, v107
	s_cselect_b32 s3, s14, s4
	s_cselect_b32 s19, s15, s5
	s_and_b64 s[0:1], vcc, exec
	v_mov_b32_e32 v35, 0x3e38aa3b
	s_cselect_b32 s1, s13, s19
	s_cselect_b32 s0, s12, s3
	v_lshlrev_b32_e32 v34, 2, v34
	v_cndmask_b32_e32 v38, 1.0, v35, vcc
	v_mov_b32_e32 v34, v204
	v_mov_b32_e32 v35, v205
	v_mov_b32_e32 v36, v206
	v_mov_b32_e32 v37, v207
	s_cmp_gt_i32 s17, 1
	v_and_or_b32 v40, s2, 48, v107
	s_mul_i32 s16, s16, 0x9000
	s_cselect_b64 s[2:3], -1, 0
	s_cmp_lt_i32 s17, 2
	s_mov_b64 s[0:1], -1
	s_waitcnt vmcnt(0)
	v_add_f32_e32 v41, v34, v30
	v_add_f32_e32 v30, v36, v32
	v_add_f32_e32 v39, v35, v31
	v_fma_mixlo_f16 v31, v38, v41, 0
	v_pk_mov_b32 v[42:43], v[38:39], v[30:31] op_sel:[1,0]
	v_add_f32_e32 v32, v37, v33
	v_pk_mul_f32 v[42:43], v[38:39], v[42:43] op_sel_hi:[0,1]
	v_fma_mixlo_f16 v32, v38, v32, 0
	v_cvt_pk_f16_f32 v33, v42, v43
	s_cbranch_scc1 .LBB1_72
	v_mul_u32_u24_e32 v30, 0x210, v40
	v_add3_u32 v30, s16, v109, v30
	s_mov_b64 s[0:1], 0
	ds_write_b16 v30, v31
	ds_write_b16 v30, v33 offset:528
	ds_write_b16_d16_hi v30, v33 offset:1056
	ds_write_b16 v30, v32 offset:1584

.LBB1_86:
	s_add_i32 s0, s37, 0x80
	s_lshr_b32 s2, s0, 6
	s_add_i32 s0, s0, s18
	s_ashr_i32 s16, s0, 10
	s_and_b32 s1, s0, 0x3f0
	s_cmpk_lt_u32 s0, 0x400
	s_cselect_b64 vcc, -1, 0
	s_cmp_eq_u32 s16, 1
	v_or_b32_e32 v18, s1, v107
	s_cselect_b32 s3, s14, s4
	s_cselect_b32 s4, s15, s5
	s_and_b64 s[0:1], vcc, exec
	v_mov_b32_e32 v19, 0x3e38aa3b
	s_cselect_b32 s1, s13, s4
	s_cselect_b32 s0, s12, s3
	v_lshlrev_b32_e32 v18, 2, v18
	v_cndmask_b32_e32 v22, 1.0, v19, vcc
	v_mov_b32_e32 v18, v208
	v_mov_b32_e32 v19, v209
	v_mov_b32_e32 v20, v210
	v_mov_b32_e32 v21, v211
	s_cmp_gt_i32 s16, 1
	s_mul_i32 s4, s2, 0x9000
	s_cselect_b64 s[2:3], -1, 0
	s_cmp_lt_i32 s16, 2
	s_mov_b64 s[0:1], -1
	s_waitcnt vmcnt(0)
	v_add_f32_e32 v24, v18, v14
	v_add_f32_e32 v14, v20, v16
	v_add_f32_e32 v23, v19, v15
	v_fma_mixlo_f16 v15, v22, v24, 0
	v_pk_mov_b32 v[24:25], v[22:23], v[14:15] op_sel:[1,0]
	v_add_f32_e32 v16, v21, v17
	v_pk_mul_f32 v[24:25], v[22:23], v[24:25] op_sel_hi:[0,1]
	v_fma_mixlo_f16 v16, v22, v16, 0
	v_cvt_pk_f16_f32 v17, v24, v25
	s_cbranch_scc1 .LBB1_88
	v_mul_u32_u24_e32 v14, 0x210, v106
	v_add3_u32 v14, s4, v109, v14
	s_mov_b64 s[0:1], 0
	ds_write_b16 v14, v15
	ds_write_b16 v14, v17 offset:528
	ds_write_b16_d16_hi v14, v17 offset:1056
	ds_write_b16 v14, v16 offset:1584

	.amdhsa_kernel _Z15qkv_gemm_kernelPKDF16_S0_PKfS2_S2_PDF16_S3_S3_
		.amdhsa_group_segment_fixed_size 118784
		.amdhsa_private_segment_fixed_size 0
		.amdhsa_kernarg_size 64
		.amdhsa_user_sgpr_count 2
		.amdhsa_user_sgpr_dispatch_ptr 0
		.amdhsa_user_sgpr_queue_ptr 0
		.amdhsa_user_sgpr_kernarg_segment_ptr 1
		.amdhsa_user_sgpr_dispatch_id 0
		.amdhsa_user_sgpr_kernarg_preload_length 0
		.amdhsa_user_sgpr_kernarg_preload_offset 0
		.amdhsa_user_sgpr_private_segment_size 0
		.amdhsa_uses_dynamic_stack 0
		.amdhsa_enable_private_segment 0
		.amdhsa_system_sgpr_workgroup_id_x 1
		.amdhsa_system_sgpr_workgroup_id_y 0
		.amdhsa_system_sgpr_workgroup_id_z 0
		.amdhsa_system_sgpr_workgroup_info 0
		.amdhsa_system_vgpr_workitem_id 0
		.amdhsa_next_free_vgpr 212
		.amdhsa_next_free_sgpr 96
		.amdhsa_accum_offset 212
		.amdhsa_reserve_vcc 1
		.amdhsa_float_round_mode_32 0
		.amdhsa_float_round_mode_16_64 0
		.amdhsa_float_denorm_mode_32 3
		.amdhsa_float_denorm_mode_16_64 3
		.amdhsa_dx10_clamp 1
		.amdhsa_ieee_mode 1
		.amdhsa_fp16_overflow 0
		.amdhsa_tg_split 0
		.amdhsa_exception_fp_ieee_invalid_op 0
		.amdhsa_exception_fp_denorm_src 0
		.amdhsa_exception_fp_ieee_div_zero 0
		.amdhsa_exception_fp_ieee_overflow 0
		.amdhsa_exception_fp_ieee_underflow 0
		.amdhsa_exception_fp_ieee_inexact 0
		.amdhsa_exception_int_div_zero 0
	.end_amdhsa_kernel

	.text
	.p2alignl 8, 3212836864
	.fill 256, 4, 3212836864

amdhsa.kernels:
  - .agpr_count:     0
    .args:
      - .actual_access:  read_only
        .address_space:  global
        .offset:         0
        .size:           8
        .value_kind:     global_buffer
      - .actual_access:  read_only
        .address_space:  global
        .offset:         8
        .size:           8
        .value_kind:     global_buffer
      - .actual_access:  read_only
        .address_space:  global
        .offset:         16
        .size:           8
        .value_kind:     global_buffer
      - .actual_access:  read_only
        .address_space:  global
        .offset:         24
        .size:           8
        .value_kind:     global_buffer
      - .actual_access:  read_only
        .address_space:  global
        .offset:         32
        .size:           8
        .value_kind:     global_buffer
      - .actual_access:  read_only
        .address_space:  global
        .offset:         40
        .size:           8
        .value_kind:     global_buffer
      - .actual_access:  write_only
        .address_space:  global
        .offset:         48
        .size:           8
        .value_kind:     global_buffer
      - .actual_access:  write_only
        .address_space:  global
        .offset:         56
        .size:           8
        .value_kind:     global_buffer
      - .actual_access:  write_only
        .address_space:  global
        .offset:         64
        .size:           8
        .value_kind:     global_buffer
    .group_segment_fixed_size: 9216
    .kernarg_segment_align: 8
    .kernarg_segment_size: 72
    .language:       OpenCL C
    .language_version:
      - 2
      - 0
    .max_flat_workgroup_size: 256
    .name:           _Z11prep_kernelPKfS0_S0_S0_S0_S0_PDF16_S1_S1_
    .private_segment_fixed_size: 0
    .sgpr_count:     22
    .sgpr_spill_count: 0
    .symbol:         _Z11prep_kernelPKfS0_S0_S0_S0_S0_PDF16_S1_S1_.kd
    .uniform_work_group_size: 1
    .uses_dynamic_stack: false
    .vgpr_count:     38
    .vgpr_spill_count: 0
    .wavefront_size: 64
  - .agpr_count:     0
    .args:
      - .address_space:  global
        .offset:         0
        .size:           8
        .value_kind:     global_buffer
      - .address_space:  global
        .offset:         8
        .size:           8
        .value_kind:     global_buffer
      - .actual_access:  read_only
        .address_space:  global
        .offset:         16
        .size:           8
        .value_kind:     global_buffer
      - .actual_access:  read_only
        .address_space:  global
        .offset:         24
        .size:           8
        .value_kind:     global_buffer
      - .actual_access:  read_only
        .address_space:  global
        .offset:         32
        .size:           8
        .value_kind:     global_buffer
      - .actual_access:  write_only
        .address_space:  global
        .offset:         40
        .size:           8
        .value_kind:     global_buffer
      - .actual_access:  write_only
        .address_space:  global
        .offset:         48
        .size:           8
        .value_kind:     global_buffer
      - .actual_access:  write_only
        .address_space:  global
        .offset:         56
        .size:           8
        .value_kind:     global_buffer
    .group_segment_fixed_size: 118784
    .kernarg_segment_align: 8
    .kernarg_segment_size: 64
    .language:       OpenCL C
    .language_version:
      - 2
      - 0
    .max_flat_workgroup_size: 512
    .name:           _Z15qkv_gemm_kernelPKDF16_S0_PKfS2_S2_PDF16_S3_S3_
    .private_segment_fixed_size: 0
    .sgpr_count:     49
    .sgpr_spill_count: 0
    .symbol:         _Z15qkv_gemm_kernelPKDF16_S0_PKfS2_S2_PDF16_S3_S3_.kd
    .uniform_work_group_size: 1
    .uses_dynamic_stack: false
    .vgpr_count:     212
    .vgpr_spill_count: 0
    .wavefront_size: 64
  - .agpr_count:     0
    .args:
      - .actual_access:  read_only
        .address_space:  global
        .offset:         0
        .size:           8
        .value_kind:     global_buffer
      - .address_space:  global
        .offset:         8
        .size:           8
        .value_kind:     global_buffer
      - .address_space:  global
        .offset:         16
        .size:           8
        .value_kind:     global_buffer
      - .address_space:  global
        .offset:         24
        .size:           8
        .value_kind:     global_buffer
      - .actual_access:  write_only
        .address_space:  global
        .offset:         32
        .size:           8
        .value_kind:     global_buffer
    .group_segment_fixed_size: 163840
    .kernarg_segment_align: 8
    .kernarg_segment_size: 40
    .language:       OpenCL C
    .language_version:
      - 2
      - 0
    .max_flat_workgroup_size: 512
    .name:           _Z11attn_kernelPKDF16_S0_S0_S0_PDF16_
    .private_segment_fixed_size: 0
    .sgpr_count:     106
    .sgpr_spill_count: 42
    .symbol:         _Z11attn_kernelPKDF16_S0_S0_S0_PDF16_.kd
    .uniform_work_group_size: 1
    .uses_dynamic_stack: false
    .vgpr_count:     253
    .vgpr_spill_count: 0
    .wavefront_size: 64
  - .agpr_count:     32
    .args:
      - .address_space:  global
        .offset:         0
        .size:           8
        .value_kind:     global_buffer
      - .address_space:  global
        .offset:         8
        .size:           8
        .value_kind:     global_buffer
      - .offset:         16
        .size:           4
        .value_kind:     by_value
      - .offset:         20
        .size:           4
        .value_kind:     by_value
      - .actual_access:  read_only
        .address_space:  global
        .offset:         24
        .size:           8
        .value_kind:     global_buffer
      - .actual_access:  read_only
        .address_space:  global
        .offset:         32
        .size:           8
        .value_kind:     global_buffer
      - .actual_access:  read_only
        .address_space:  global
        .offset:         40
        .size:           8
        .value_kind:     global_buffer
      - .actual_access:  read_only
        .address_space:  global
        .offset:         48
        .size:           8
        .value_kind:     global_buffer
      - .actual_access:  read_only
        .address_space:  global
        .offset:         56
        .size:           8
        .value_kind:     global_buffer
      - .actual_access:  read_only
        .address_space:  global
        .offset:         64
        .size:           8
        .value_kind:     global_buffer
      - .actual_access:  write_only
        .address_space:  global
        .offset:         72
        .size:           8
        .value_kind:     global_buffer
      - .offset:         80
        .size:           4
        .value_kind:     hidden_block_count_x
      - .offset:         84
        .size:           4
        .value_kind:     hidden_block_count_y
      - .offset:         88
        .size:           4
        .value_kind:     hidden_block_count_z
      - .offset:         92
        .size:           2
        .value_kind:     hidden_group_size_x
      - .offset:         94
        .size:           2
        .value_kind:     hidden_group_size_y
      - .offset:         96
        .size:           2
        .value_kind:     hidden_group_size_z
      - .offset:         98
        .size:           2
        .value_kind:     hidden_remainder_x
      - .offset:         100
        .size:           2
        .value_kind:     hidden_remainder_y
      - .offset:         102
        .size:           2
        .value_kind:     hidden_remainder_z
      - .offset:         120
        .size:           8
        .value_kind:     hidden_global_offset_x
      - .offset:         128
        .size:           8
        .value_kind:     hidden_global_offset_y
      - .offset:         136
        .size:           8
        .value_kind:     hidden_global_offset_z
      - .offset:         144
        .size:           2
        .value_kind:     hidden_grid_dims
    .group_segment_fixed_size: 49152
    .kernarg_segment_align: 8
    .kernarg_segment_size: 336
    .language:       OpenCL C
    .language_version:
      - 2
      - 0
    .max_flat_workgroup_size: 256
    .name:           _Z11gemm_kernelILi1ELi1EEvPKDF16_S1_iiPKfS3_S3_PDF16_S4_S4_Pf
    .private_segment_fixed_size: 0
    .sgpr_count:     28
    .sgpr_spill_count: 0
    .symbol:         _Z11gemm_kernelILi1ELi1EEvPKDF16_S1_iiPKfS3_S3_PDF16_S4_S4_Pf.kd
    .uniform_work_group_size: 1
    .uses_dynamic_stack: false
    .vgpr_count:     96
    .vgpr_spill_count: 0
    .wavefront_size: 64
